# loop-head placement: GEMM K-loop heads and PEER retrieval loop heads on 64-byte boundaries
# baseline (speedup 1.0000x reference)
; template <class Epi, class Sched, bool ALIGN_EPI = false, bool SP2 = false>
; __device__ __forceinline__ void gemm_phase(PG8_LAS unsigned char* lds, const Gemm g, const Sched& S, const Epi& E) {
;     ...
;     for (;;) {
;         const bool has_next = S.next(ui + 1, nxt);
;         const char* nA = has_next ? (const char*)g.A + (size_t)nxt.pm * tstep : cA; const char* nB = has_next ? (const char*)g.Bt + (size_t)nxt.pn * tstep : cB;
;         for (int t = 0; t < nt; t += 2) {
;     ...
; #pragma unroll
;         for (int a = 0; a < 2; ++a)
; #pragma unroll
;             for (int b = 0; b < 2; ++b)
; #pragma unroll
;                 for (int m = 0; m < 4; ++m)
; #pragma unroll
;                     for (int n = 0; n < 2; ++n) acc[a][b][m][n] = (f32x4){0.f, 0.f, 0.f, 0.f};
;         cur = nxt; cA = nA; cB = nB; ++ui;
.LBB0_375:
	s_ashr_i32 s23, s22, 31
	s_lshl_b64 s[24:25], s[22:23], 19
	s_add_u32 s24, s84, s24
	s_addc_u32 s25, s85, s25
	s_and_b64 s[26:27], s[82:83], exec
	s_cselect_b32 s9, s25, s7
	s_cselect_b32 s23, s24, s6
	s_ashr_i32 s21, s20, 31
	s_lshl_b64 s[26:27], s[20:21], 19
	s_add_u32 s26, s44, s26
	s_addc_u32 s27, s45, s27
	s_and_b64 s[34:35], s[82:83], exec
	s_cselect_b32 s21, s27, s31
	s_cselect_b32 s29, s26, s30
	s_add_u32 s6, s6, 0x40080
	s_addc_u32 s7, s7, 0
	s_add_u32 s33, s30, 0x100
	v_mov_b32_e32 v64, 0
	s_addc_u32 s36, s31, 0
	s_mov_b32 s37, -2
	v_mov_b32_e32 v65, v64
	v_mov_b32_e32 v66, v64
	v_mov_b32_e32 v67, v64
	v_mov_b32_e32 v68, v64
	v_mov_b32_e32 v69, v64
	v_mov_b32_e32 v70, v64
	v_mov_b32_e32 v71, v64
	v_mov_b32_e32 v72, v64
	v_mov_b32_e32 v73, v64
	v_mov_b32_e32 v74, v64
	v_mov_b32_e32 v75, v64
	v_mov_b32_e32 v76, v64
	v_mov_b32_e32 v77, v64
	v_mov_b32_e32 v78, v64
	v_mov_b32_e32 v79, v64
	v_mov_b32_e32 v80, v64
	v_mov_b32_e32 v81, v64
	v_mov_b32_e32 v82, v64
	v_mov_b32_e32 v83, v64
	v_mov_b32_e32 v84, v64
	v_mov_b32_e32 v85, v64
	v_mov_b32_e32 v86, v64
	v_mov_b32_e32 v87, v64
	v_mov_b32_e32 v88, v64
	v_mov_b32_e32 v89, v64
	v_mov_b32_e32 v90, v64
	v_mov_b32_e32 v91, v64
	v_mov_b32_e32 v92, v64
	v_mov_b32_e32 v93, v64
	v_mov_b32_e32 v94, v64
	v_mov_b32_e32 v95, v64
	v_mov_b32_e32 v0, v64
	v_mov_b32_e32 v1, v64
	v_mov_b32_e32 v2, v64
	v_mov_b32_e32 v3, v64
	v_mov_b32_e32 v4, v64
	v_mov_b32_e32 v5, v64
	v_mov_b32_e32 v6, v64
	v_mov_b32_e32 v7, v64
	v_mov_b32_e32 v8, v64
	v_mov_b32_e32 v9, v64
	v_mov_b32_e32 v10, v64
	v_mov_b32_e32 v11, v64
	v_mov_b32_e32 v12, v64
	v_mov_b32_e32 v13, v64
	v_mov_b32_e32 v14, v64
	v_mov_b32_e32 v15, v64
	v_mov_b32_e32 v16, v64
	v_mov_b32_e32 v17, v64
	v_mov_b32_e32 v18, v64
	v_mov_b32_e32 v19, v64
	v_mov_b32_e32 v20, v64
	v_mov_b32_e32 v21, v64
	v_mov_b32_e32 v22, v64
	v_mov_b32_e32 v23, v64
	v_mov_b32_e32 v24, v64
	v_mov_b32_e32 v25, v64
	v_mov_b32_e32 v26, v64
	v_mov_b32_e32 v27, v64
	v_mov_b32_e32 v28, v64
	v_mov_b32_e32 v29, v64
	v_mov_b32_e32 v30, v64
	v_mov_b32_e32 v31, v64
	v_mov_b32_e32 v96, v64
	v_mov_b32_e32 v97, v64
	v_mov_b32_e32 v98, v64
	v_mov_b32_e32 v99, v64
	v_mov_b32_e32 v100, v64
	v_mov_b32_e32 v101, v64
	v_mov_b32_e32 v102, v64
	v_mov_b32_e32 v103, v64
	v_mov_b32_e32 v104, v64
	v_mov_b32_e32 v105, v64
	v_mov_b32_e32 v106, v64
	v_mov_b32_e32 v107, v64
	v_mov_b32_e32 v108, v64
	v_mov_b32_e32 v109, v64
	v_mov_b32_e32 v110, v64
	v_mov_b32_e32 v111, v64
	v_mov_b32_e32 v112, v64
	v_mov_b32_e32 v113, v64
	v_mov_b32_e32 v114, v64
	v_mov_b32_e32 v115, v64
	v_mov_b32_e32 v116, v64
	v_mov_b32_e32 v117, v64
	v_mov_b32_e32 v118, v64
	v_mov_b32_e32 v119, v64
	v_mov_b32_e32 v120, v64
	v_mov_b32_e32 v121, v64
	v_mov_b32_e32 v122, v64
	v_mov_b32_e32 v123, v64
	v_mov_b32_e32 v124, v64
	v_mov_b32_e32 v125, v64
	v_mov_b32_e32 v126, v64
	v_mov_b32_e32 v127, v64
	v_mov_b32_e32 v32, v64
	v_mov_b32_e32 v33, v64
	v_mov_b32_e32 v34, v64
	v_mov_b32_e32 v35, v64
	v_mov_b32_e32 v36, v64
	v_mov_b32_e32 v37, v64
	v_mov_b32_e32 v38, v64
	v_mov_b32_e32 v39, v64
	v_mov_b32_e32 v40, v64
	v_mov_b32_e32 v41, v64
	v_mov_b32_e32 v42, v64
	v_mov_b32_e32 v43, v64
	v_mov_b32_e32 v44, v64
	v_mov_b32_e32 v45, v64
	v_mov_b32_e32 v46, v64
	v_mov_b32_e32 v47, v64
	v_mov_b32_e32 v48, v64
	v_mov_b32_e32 v49, v64
	v_mov_b32_e32 v50, v64
	v_mov_b32_e32 v51, v64
	v_mov_b32_e32 v52, v64
	v_mov_b32_e32 v53, v64
	v_mov_b32_e32 v54, v64
	v_mov_b32_e32 v55, v64
	v_mov_b32_e32 v56, v64
	v_mov_b32_e32 v57, v64
	v_mov_b32_e32 v58, v64
	v_mov_b32_e32 v59, v64
	v_mov_b32_e32 v60, v64
	v_mov_b32_e32 v61, v64
	v_mov_b32_e32 v62, v64
	v_mov_b32_e32 v63, v64
	.p2align	6

; template <class Epi, class Sched, bool ALIGN_EPI = false, bool SP2 = false>
; __device__ __forceinline__ void gemm_phase(PG8_LAS unsigned char* lds, const Gemm g, const Sched& S, const Epi& E) {
;     ...
;     for (;;) {
;         const bool has_next = S.next(ui + 1, nxt);
;         const char* nA = has_next ? (const char*)g.A + (size_t)nxt.pm * tstep : cA; const char* nB = has_next ? (const char*)g.Bt + (size_t)nxt.pn * tstep : cB;
;         for (int t = 0; t < nt; t += 2) {
;     ...
; #pragma unroll
;         for (int a = 0; a < 2; ++a)
; #pragma unroll
;             for (int b = 0; b < 2; ++b)
; #pragma unroll
;                 for (int m = 0; m < 4; ++m)
; #pragma unroll
;                     for (int n = 0; n < 2; ++n) acc[a][b][m][n] = (f32x4){0.f, 0.f, 0.f, 0.f};
;         cur = nxt; cA = nA; cB = nB; ++ui;
.LBB0_662:
	s_ashr_i32 s19, s18, 31
	s_lshl_b64 s[20:21], s[18:19], 19
	v_readlane_b32 s22, v237, 45
	v_readlane_b32 s23, v237, 46
	s_add_u32 s20, s22, s20
	s_addc_u32 s21, s23, s21
	s_and_b64 s[22:23], s[4:5], exec
	s_cselect_b32 s19, s21, s27
	s_cselect_b32 s25, s20, s26
	s_ashr_i32 s17, s16, 31
	s_lshl_b64 s[22:23], s[16:17], 19
	s_add_u32 s22, s33, s22
	s_addc_u32 s23, s34, s23
	s_and_b64 s[30:31], s[4:5], exec
	s_cselect_b32 s17, s23, s29
	s_cselect_b32 s48, s22, s28
	s_add_u32 s26, s26, 0x40080
	s_addc_u32 s27, s27, 0
	s_add_u32 s49, s28, 0x100
	v_mov_b32_e32 v0, 0
	s_addc_u32 s50, s29, 0
	s_mov_b32 s51, -2
	s_waitcnt lgkmcnt(0)
	v_mov_b32_e32 v1, v0
	v_mov_b32_e32 v2, v0
	v_mov_b32_e32 v3, v0
	v_mov_b32_e32 v4, v0
	v_mov_b32_e32 v5, v0
	v_mov_b32_e32 v6, v0
	v_mov_b32_e32 v7, v0
	v_mov_b32_e32 v16, v0
	v_mov_b32_e32 v17, v0
	v_mov_b32_e32 v18, v0
	v_mov_b32_e32 v19, v0
	v_mov_b32_e32 v20, v0
	v_mov_b32_e32 v21, v0
	v_mov_b32_e32 v22, v0
	v_mov_b32_e32 v23, v0
	v_mov_b32_e32 v32, v0
	v_mov_b32_e32 v33, v0
	v_mov_b32_e32 v34, v0
	v_mov_b32_e32 v35, v0
	v_mov_b32_e32 v36, v0
	v_mov_b32_e32 v37, v0
	v_mov_b32_e32 v38, v0
	v_mov_b32_e32 v39, v0
	v_mov_b32_e32 v48, v0
	v_mov_b32_e32 v49, v0
	v_mov_b32_e32 v50, v0
	v_mov_b32_e32 v51, v0
	v_mov_b32_e32 v52, v0
	v_mov_b32_e32 v53, v0
	v_mov_b32_e32 v54, v0
	v_mov_b32_e32 v55, v0
	v_mov_b32_e32 v8, v0
	v_mov_b32_e32 v9, v0
	v_mov_b32_e32 v10, v0
	v_mov_b32_e32 v11, v0
	v_mov_b32_e32 v12, v0
	v_mov_b32_e32 v13, v0
	v_mov_b32_e32 v14, v0
	v_mov_b32_e32 v15, v0
	v_mov_b32_e32 v24, v0
	v_mov_b32_e32 v25, v0
	v_mov_b32_e32 v26, v0
	v_mov_b32_e32 v27, v0
	v_mov_b32_e32 v28, v0
	v_mov_b32_e32 v29, v0
	v_mov_b32_e32 v30, v0
	v_mov_b32_e32 v31, v0
	v_mov_b32_e32 v40, v0
	v_mov_b32_e32 v41, v0
	v_mov_b32_e32 v42, v0
	v_mov_b32_e32 v43, v0
	v_mov_b32_e32 v44, v0
	v_mov_b32_e32 v45, v0
	v_mov_b32_e32 v46, v0
	v_mov_b32_e32 v47, v0
	v_mov_b32_e32 v56, v0
	v_mov_b32_e32 v57, v0
	v_mov_b32_e32 v58, v0
	v_mov_b32_e32 v59, v0
	v_mov_b32_e32 v60, v0
	v_mov_b32_e32 v61, v0
	v_mov_b32_e32 v62, v0
	v_mov_b32_e32 v63, v0
	s_waitcnt vmcnt(0)
	v_mov_b32_e32 v64, v0
	v_mov_b32_e32 v65, v0
	v_mov_b32_e32 v66, v0
	v_mov_b32_e32 v67, v0
	v_mov_b32_e32 v68, v0
	v_mov_b32_e32 v69, v0
	v_mov_b32_e32 v70, v0
	v_mov_b32_e32 v71, v0
	v_mov_b32_e32 v80, v0
	v_mov_b32_e32 v81, v0
	v_mov_b32_e32 v82, v0
	v_mov_b32_e32 v83, v0
	v_mov_b32_e32 v84, v0
	v_mov_b32_e32 v85, v0
	v_mov_b32_e32 v86, v0
	v_mov_b32_e32 v87, v0
	v_mov_b32_e32 v96, v0
	v_mov_b32_e32 v97, v0
	v_mov_b32_e32 v98, v0
	v_mov_b32_e32 v99, v0
	v_mov_b32_e32 v100, v0
	v_mov_b32_e32 v101, v0
	v_mov_b32_e32 v102, v0
	v_mov_b32_e32 v103, v0
	v_mov_b32_e32 v112, v0
	v_mov_b32_e32 v113, v0
	v_mov_b32_e32 v114, v0
	v_mov_b32_e32 v115, v0
	v_mov_b32_e32 v116, v0
	v_mov_b32_e32 v117, v0
	v_mov_b32_e32 v118, v0
	v_mov_b32_e32 v119, v0
	v_mov_b32_e32 v72, v0
	v_mov_b32_e32 v73, v0
	v_mov_b32_e32 v74, v0
	v_mov_b32_e32 v75, v0
	v_mov_b32_e32 v76, v0
	v_mov_b32_e32 v77, v0
	v_mov_b32_e32 v78, v0
	v_mov_b32_e32 v79, v0
	v_mov_b32_e32 v88, v0
	v_mov_b32_e32 v89, v0
	v_mov_b32_e32 v90, v0
	v_mov_b32_e32 v91, v0
	v_mov_b32_e32 v92, v0
	v_mov_b32_e32 v93, v0
	v_mov_b32_e32 v94, v0
	v_mov_b32_e32 v95, v0
	v_mov_b32_e32 v104, v0
	v_mov_b32_e32 v105, v0
	v_mov_b32_e32 v106, v0
	v_mov_b32_e32 v107, v0
	v_mov_b32_e32 v108, v0
	v_mov_b32_e32 v109, v0
	v_mov_b32_e32 v110, v0
	v_mov_b32_e32 v111, v0
	v_mov_b32_e32 v120, v0
	v_mov_b32_e32 v121, v0
	v_mov_b32_e32 v122, v0
	v_mov_b32_e32 v123, v0
	v_mov_b32_e32 v124, v0
	v_mov_b32_e32 v125, v0
	v_mov_b32_e32 v126, v0
	v_mov_b32_e32 v127, v0
	.p2align	6

; template <class Epi, class Sched, bool ALIGN_EPI = false, bool SP2 = false>
; __device__ __forceinline__ void gemm_phase(PG8_LAS unsigned char* lds, const Gemm g, const Sched& S, const Epi& E) {
;     ...
;     for (;;) {
;         const bool has_next = S.next(ui + 1, nxt);
;         const char* nA = has_next ? (const char*)g.A + (size_t)nxt.pm * tstep : cA; const char* nB = has_next ? (const char*)g.Bt + (size_t)nxt.pn * tstep : cB;
;         for (int t = 0; t < nt; t += 2) {
;     ...
; #pragma unroll
;         for (int a = 0; a < 2; ++a)
; #pragma unroll
;             for (int b = 0; b < 2; ++b)
; #pragma unroll
;                 for (int m = 0; m < 4; ++m)
; #pragma unroll
;                     for (int n = 0; n < 2; ++n) acc[a][b][m][n] = (f32x4){0.f, 0.f, 0.f, 0.f};
;         cur = nxt; cA = nA; cB = nB; ++ui;
.LBB0_757:
	s_ashr_i32 s17, s16, 31
	s_lshl_b64 s[18:19], s[16:17], 19
	s_add_u32 s18, s84, s18
	s_addc_u32 s19, s85, s19
	s_and_b64 s[20:21], s[2:3], exec
	s_cselect_b32 s17, s19, s23
	s_cselect_b32 s44, s18, s22
	s_ashr_i32 s15, s14, 31
	s_lshl_b64 s[20:21], s[14:15], 19
	s_add_u32 s20, s29, s20
	s_addc_u32 s21, s30, s21
	s_and_b64 s[26:27], s[2:3], exec
	s_cselect_b32 s15, s21, s25
	s_cselect_b32 s45, s20, s24
	s_add_u32 s22, s22, 0x40080
	s_addc_u32 s23, s23, 0
	s_add_u32 s46, s24, 0x100
	v_mov_b32_e32 v0, 0
	s_addc_u32 s47, s25, 0
	s_mov_b32 s48, -2
	v_mov_b32_e32 v1, v0
	v_mov_b32_e32 v2, v0
	v_mov_b32_e32 v3, v0
	v_mov_b32_e32 v4, v0
	v_mov_b32_e32 v5, v0
	v_mov_b32_e32 v6, v0
	v_mov_b32_e32 v7, v0
	v_mov_b32_e32 v16, v0
	v_mov_b32_e32 v17, v0
	v_mov_b32_e32 v18, v0
	v_mov_b32_e32 v19, v0
	v_mov_b32_e32 v20, v0
	v_mov_b32_e32 v21, v0
	v_mov_b32_e32 v22, v0
	v_mov_b32_e32 v23, v0
	v_mov_b32_e32 v32, v0
	v_mov_b32_e32 v33, v0
	v_mov_b32_e32 v34, v0
	v_mov_b32_e32 v35, v0
	v_mov_b32_e32 v36, v0
	v_mov_b32_e32 v37, v0
	v_mov_b32_e32 v38, v0
	v_mov_b32_e32 v39, v0
	v_mov_b32_e32 v48, v0
	v_mov_b32_e32 v49, v0
	v_mov_b32_e32 v50, v0
	v_mov_b32_e32 v51, v0
	v_mov_b32_e32 v52, v0
	v_mov_b32_e32 v53, v0
	v_mov_b32_e32 v54, v0
	v_mov_b32_e32 v55, v0
	v_mov_b32_e32 v8, v0
	v_mov_b32_e32 v9, v0
	v_mov_b32_e32 v10, v0
	v_mov_b32_e32 v11, v0
	v_mov_b32_e32 v12, v0
	v_mov_b32_e32 v13, v0
	v_mov_b32_e32 v14, v0
	v_mov_b32_e32 v15, v0
	v_mov_b32_e32 v24, v0
	v_mov_b32_e32 v25, v0
	v_mov_b32_e32 v26, v0
	v_mov_b32_e32 v27, v0
	v_mov_b32_e32 v28, v0
	v_mov_b32_e32 v29, v0
	v_mov_b32_e32 v30, v0
	v_mov_b32_e32 v31, v0
	v_mov_b32_e32 v40, v0
	v_mov_b32_e32 v41, v0
	v_mov_b32_e32 v42, v0
	v_mov_b32_e32 v43, v0
	v_mov_b32_e32 v44, v0
	v_mov_b32_e32 v45, v0
	v_mov_b32_e32 v46, v0
	v_mov_b32_e32 v47, v0
	v_mov_b32_e32 v56, v0
	v_mov_b32_e32 v57, v0
	v_mov_b32_e32 v58, v0
	v_mov_b32_e32 v59, v0
	v_mov_b32_e32 v60, v0
	v_mov_b32_e32 v61, v0
	v_mov_b32_e32 v62, v0
	v_mov_b32_e32 v63, v0
	v_mov_b32_e32 v64, v0
	v_mov_b32_e32 v65, v0
	v_mov_b32_e32 v66, v0
	v_mov_b32_e32 v67, v0
	v_mov_b32_e32 v68, v0
	v_mov_b32_e32 v69, v0
	v_mov_b32_e32 v70, v0
	v_mov_b32_e32 v71, v0
	v_mov_b32_e32 v80, v0
	v_mov_b32_e32 v81, v0
	v_mov_b32_e32 v82, v0
	v_mov_b32_e32 v83, v0
	v_mov_b32_e32 v84, v0
	v_mov_b32_e32 v85, v0
	v_mov_b32_e32 v86, v0
	v_mov_b32_e32 v87, v0
	v_mov_b32_e32 v96, v0
	v_mov_b32_e32 v97, v0
	v_mov_b32_e32 v98, v0
	v_mov_b32_e32 v99, v0
	v_mov_b32_e32 v100, v0
	v_mov_b32_e32 v101, v0
	v_mov_b32_e32 v102, v0
	v_mov_b32_e32 v103, v0
	v_mov_b32_e32 v112, v0
	v_mov_b32_e32 v113, v0
	v_mov_b32_e32 v114, v0
	v_mov_b32_e32 v115, v0
	v_mov_b32_e32 v116, v0
	v_mov_b32_e32 v117, v0
	v_mov_b32_e32 v118, v0
	v_mov_b32_e32 v119, v0
	v_mov_b32_e32 v72, v0
	v_mov_b32_e32 v73, v0
	v_mov_b32_e32 v74, v0
	v_mov_b32_e32 v75, v0
	v_mov_b32_e32 v76, v0
	v_mov_b32_e32 v77, v0
	v_mov_b32_e32 v78, v0
	v_mov_b32_e32 v79, v0
	v_mov_b32_e32 v88, v0
	v_mov_b32_e32 v89, v0
	v_mov_b32_e32 v90, v0
	v_mov_b32_e32 v91, v0
	v_mov_b32_e32 v92, v0
	v_mov_b32_e32 v93, v0
	v_mov_b32_e32 v94, v0
	v_mov_b32_e32 v95, v0
	v_mov_b32_e32 v104, v0
	v_mov_b32_e32 v105, v0
	v_mov_b32_e32 v106, v0
	v_mov_b32_e32 v107, v0
	v_mov_b32_e32 v108, v0
	v_mov_b32_e32 v109, v0
	v_mov_b32_e32 v110, v0
	v_mov_b32_e32 v111, v0
	v_mov_b32_e32 v120, v0
	v_mov_b32_e32 v121, v0
	v_mov_b32_e32 v122, v0
	v_mov_b32_e32 v123, v0
	v_mov_b32_e32 v124, v0
	v_mov_b32_e32 v125, v0
	v_mov_b32_e32 v126, v0
	v_mov_b32_e32 v127, v0
	.p2align	6

; #define LAS __attribute__((address_space(3)))
; __device__ __forceinline__ int opaque_i(int v) { asm volatile("" : "+v"(v)); return v; }
; __device__ __forceinline__ void phase_topk(Frame& F, const bf16_t* QP, const bf16_t* K1B, const bf16_t* K2B, unsigned short* EID, float* GATE) {
;     const int lane = opaque_i(F.lane), r32 = lane & 31, hi = lane >> 5, b = (int)blockIdx.x, h = b & 7, nbh = F.G >> 3;
;     { u32x4 kv[8];
; #pragma unroll
;       for (int k = 0; k < 8; ++k) { const int c = F.tid + k * (NWAVES * 64), sub = c >> 11, n = (c >> 4) & 127, part = c & 15; kv[k] = *(const u32x4*)((sub ? K2B : K1B) + ((size_t)h * 128 + n) * 128 + 8 * part); }
; #pragma unroll
;       for (int k = 0; k < 8; ++k) { const int c = F.tid + k * (NWAVES * 64), sub = c >> 11, n = (c >> 4) & 127, part = c & 15; *(LAS u32x4*)(F.lds + sub * TK_KSET + n * TK_KSTRIDE + 16 * part) = kv[k]; } }
;     __syncthreads();
;     LAS unsigned* I1s = (LAS unsigned*)(F.lds + TK_KBYTES + F.wave * 8192); LAS unsigned* I2s = I1s + 1024;
;     bf16x8 qn[8];
;     { const int tile0 = (b >> 3) + nbh * F.wave; const bf16_t* qrow = QP + (size_t)((tile0 < TOK / 32 ? tile0 : 0) * 32 + r32) * 2048 + h * 256 + 8 * hi;
; #pragma unroll
;       for (int kk = 0; kk < 8; ++kk) qn[kk] = *(const bf16x8*)(qrow + 16 * kk); }
;     for (int tile = (b >> 3) + nbh * F.wave; tile < TOK / 32; tile += nbh * NWAVES) {
;         const int t = tile * 32 + r32;
;         unsigned V1[16], V2[16]; unsigned h4 = (unsigned)hi << 2; asm volatile("" : "+v"(h4));
; #pragma unroll
.LBB0_819:
	v_readlane_b32 s2, v237, 4
	v_readlane_b32 s3, v237, 5
	s_cmp_lt_i32 s2, 7
	s_cselect_b64 s[2:3], -1, 0
	s_add_u32 s4, s78, 0x1e000000
	s_addc_u32 s5, s79, 0
	v_writelane_b32 v236, s4, 3
	v_lshlrev_b32_e32 v184, 3, v209
	v_lshlrev_b32_e32 v183, 4, v209
	v_writelane_b32 v236, s5, 4
	s_add_u32 s4, s78, 0x1e800000
	v_writelane_b32 v236, s4, 14
	s_addc_u32 s4, s79, 0
	s_and_b64 s[0:1], s[2:3], s[0:1]
	s_andn2_b64 vcc, exec, s[0:1]
	v_lshrrev_b32_e32 v182, 4, v209
	v_writelane_b32 v236, s4, 17
	s_cbranch_vccnz .LBB0_823
	s_add_u32 s2, s78, 0x1800000
	s_addc_u32 s3, s79, 0
	s_add_u32 s8, s78, 0x1880000
	v_readlane_b32 s11, v237, 3
	s_addc_u32 s9, s79, 0
	s_and_b32 s4, s11, 7
	s_lshl_b32 s5, s4, 14
	s_waitcnt lgkmcnt(0)
	v_and_b32_e32 v1, 0x1f80, v184
	v_or_b32_e32 v1, s5, v1
	v_lshlrev_b32_e32 v30, 1, v1
	v_mov_b32_e32 v31, 0
	v_lshl_add_u64 v[2:3], s[2:3], 0, v[30:31]
	v_and_b32_e32 v34, 0xf0, v183
	v_mov_b32_e32 v35, v31
	v_add_u32_e32 v1, 0x200, v209
	v_lshl_add_u64 v[10:11], v[2:3], 0, v[34:35]
	v_lshlrev_b32_e32 v2, 3, v1
	v_and_b32_e32 v2, 0x3f80, v2
	v_or_b32_e32 v2, s5, v2
	s_movk_i32 s10, 0x200
	v_lshlrev_b32_e32 v2, 1, v2
	v_mov_b32_e32 v3, v31
	v_mov_b32_e32 v0, v208
	v_lshl_add_u64 v[2:3], s[2:3], 0, v[2:3]
	v_or_b32_e32 v36, 0x400, v209
	v_mov_b32_e32 v14, s9
	v_mov_b32_e32 v15, s3
	v_cmp_gt_u32_e32 vcc, s10, v209
	v_lshl_add_u64 v[12:13], v[2:3], 0, v[34:35]
	global_load_dwordx4 v[2:5], v[10:11], off
	global_load_dwordx4 v[6:9], v[12:13], off
	v_lshlrev_b32_e32 v10, 3, v36
	v_add_u32_e32 v37, 0x600, v209
	v_cndmask_b32_e32 v15, v14, v15, vcc
	v_mov_b32_e32 v14, s8
	v_mov_b32_e32 v16, s2
	v_and_b32_e32 v10, 0x3f80, v10
	v_cndmask_b32_e32 v14, v14, v16, vcc
	v_lshlrev_b32_e32 v16, 3, v37
	v_lshl_add_u64 v[18:19], s[8:9], 0, v[30:31]
	v_add_u32_e32 v38, 0xa00, v209
	v_or_b32_e32 v10, s5, v10
	v_and_b32_e32 v16, 0x3f80, v16
	v_lshl_add_u64 v[26:27], v[18:19], 0, v[34:35]
	v_lshlrev_b32_e32 v18, 3, v38
	v_lshlrev_b32_e32 v10, 1, v10
	v_mov_b32_e32 v11, v31
	v_or_b32_e32 v16, s5, v16
	v_and_b32_e32 v18, 0x3f80, v18
	v_lshl_add_u64 v[10:11], s[2:3], 0, v[10:11]
	v_lshlrev_b32_e32 v16, 1, v16
	v_mov_b32_e32 v17, v31
	v_or_b32_e32 v18, s5, v18
	v_lshl_add_u64 v[10:11], v[10:11], 0, v[34:35]
	v_lshl_add_u64 v[14:15], v[14:15], 0, v[16:17]
	v_lshlrev_b32_e32 v30, 1, v18
	global_load_dwordx4 v[10:13], v[10:11], off
	v_lshl_add_u64 v[14:15], v[14:15], 0, v[34:35]
	v_lshl_add_u64 v[18:19], s[8:9], 0, v[30:31]
	v_or_b32_e32 v39, 0xc00, v209
	global_load_dwordx4 v[14:17], v[14:15], off
	v_lshl_add_u64 v[28:29], v[18:19], 0, v[34:35]
	global_load_dwordx4 v[18:21], v[26:27], off
	global_load_dwordx4 v[22:25], v[28:29], off
	v_lshlrev_b32_e32 v26, 3, v39
	v_and_b32_e32 v26, 0x3f80, v26
	v_or_b32_e32 v26, s5, v26
	v_lshlrev_b32_e32 v30, 1, v26
	v_lshl_add_u64 v[26:27], s[8:9], 0, v[30:31]
	v_add_u32_e32 v40, 0xe00, v209
	v_lshl_add_u64 v[26:27], v[26:27], 0, v[34:35]
	v_lshlrev_b32_e32 v30, 3, v40
	global_load_dwordx4 v[26:29], v[26:27], off
	v_and_b32_e32 v30, 0x3f80, v30
	v_or_b32_e32 v30, s5, v30
	v_lshlrev_b32_e32 v30, 1, v30
	v_lshl_add_u64 v[30:31], s[8:9], 0, v[30:31]
	v_lshl_add_u64 v[30:31], v[30:31], 0, v[34:35]
	global_load_dwordx4 v[30:33], v[30:31], off
	v_lshrrev_b32_e32 v1, 4, v1
	v_mul_u32_u24_e32 v35, 0x110, v182
	v_lshrrev_b32_e32 v36, 4, v36
	v_mul_u32_u24_e32 v1, 0x110, v1
	v_add3_u32 v35, 0, v35, v34
	v_mul_u32_u24_e32 v36, 0x110, v36
	v_add3_u32 v1, 0, v1, v34
	v_add3_u32 v36, 0, v36, v34
	s_mov_b32 s2, 0x8800
	s_ashr_i32 s5, s11, 3
	s_mov_b32 s3, 0
	s_waitcnt vmcnt(0)
	ds_write_b128 v35, v[2:5]
	ds_write_b128 v1, v[6:9]
	ds_write_b128 v36, v[10:13]
	v_lshrrev_b32_e32 v1, 11, v37
	v_bfe_u32 v2, v37, 4, 7
	v_mad_u32_u24 v1, v1, s2, 0
	v_mul_u32_u24_e32 v2, 0x110, v2
	v_add3_u32 v1, v1, v2, v34
	ds_write_b128 v1, v[14:17]
	ds_write_b128 v35, v[18:21] offset:34816
	v_bfe_u32 v1, v38, 4, 7
	v_mul_u32_u24_e32 v1, 0x110, v1
	v_add3_u32 v1, 0, v1, v34
	ds_write_b128 v1, v[22:25] offset:34816
	v_bfe_u32 v1, v39, 4, 7
	v_mul_u32_u24_e32 v1, 0x110, v1
	v_add3_u32 v1, 0, v1, v34
	v_bfe_u32 v2, v40, 4, 7
	v_mul_u32_u24_e32 v2, 0x110, v2
	ds_write_b128 v1, v[26:29] offset:34816
	v_lshrrev_b32_e32 v1, 11, v40
	v_mad_u32_u24 v1, v1, s2, 0
	s_ashr_i32 s2, s72, 3
	s_mul_i32 s2, s2, s74
	s_add_i32 s33, s2, s5
	v_add3_u32 v1, v1, v2, v34
	s_cmpk_gt_i32 s33, 0x3ff
	ds_write_b128 v1, v[30:33]
	s_waitcnt lgkmcnt(0)
	s_barrier
	s_cbranch_scc1 .LBB0_823
	v_and_b32_e32 v88, 31, v0
	v_lshl_or_b32 v80, s33, 5, v88
	v_ashrrev_i32_e32 v1, 5, v0
	v_ashrrev_i32_e32 v81, 31, v80
	v_lshlrev_b32_e32 v2, 3, v1
	v_lshlrev_b64 v[4:5], 12, v[80:81]
	v_ashrrev_i32_e32 v3, 31, v2
	v_lshl_add_u64 v[4:5], s[96:97], 0, v[4:5]
	s_lshl_b32 s2, s4, 9
	v_lshl_add_u64 v[4:5], v[4:5], 0, s[2:3]
	v_lshlrev_b64 v[6:7], 1, v[2:3]
	v_lshl_add_u64 v[4:5], v[4:5], 0, v[6:7]
	global_load_dwordx4 v[16:19], v[4:5], off offset:224
	global_load_dwordx4 v[20:23], v[4:5], off offset:192
	global_load_dwordx4 v[24:27], v[4:5], off offset:160
	global_load_dwordx4 v[28:31], v[4:5], off offset:128
	global_load_dwordx4 v[32:35], v[4:5], off offset:96
	global_load_dwordx4 v[36:39], v[4:5], off offset:64
	global_load_dwordx4 v[40:43], v[4:5], off offset:32
	global_load_dwordx4 v[44:47], v[4:5], off
	s_lshl_b32 s3, s74, 13
	s_add_i32 s3, s3, 0
	s_add_i32 s3, s3, 0x11000
	s_and_b32 s8, s72, -8
	s_add_u32 s10, s96, s2
	s_addc_u32 s11, s97, 0
	s_lshl_b32 s5, s4, 5
	v_readlane_b32 s12, v236, 3
	v_readlane_b32 s13, v236, 4
	s_add_u32 s12, s12, s5
	s_addc_u32 s13, s13, 0
	s_lshl_b32 s4, s4, 6
	v_readlane_b32 s5, v236, 14
	s_add_u32 s4, s5, s4
	v_readlane_b32 s5, v236, 17
	v_lshlrev_b32_e32 v89, 2, v1
	v_lshlrev_b32_e32 v1, 4, v1
	v_lshl_add_u32 v90, v0, 2, s3
	v_cmp_gt_u32_e64 s[2:3], 32, v0
	s_addc_u32 s5, s5, 0
	v_mul_u32_u24_e32 v0, 0x110, v88
	v_lshl_add_u64 v[84:85], v[2:3], 2, s[4:5]
	v_add3_u32 v91, 0, v0, v1
	s_lshl_b32 s4, s72, 5
	v_mbcnt_lo_u32_b32 v0, -1, 0
	v_lshl_add_u64 v[82:83], s[12:13], 0, v[6:7]
	v_lshl_add_u64 v[86:87], s[10:11], 0, v[6:7]
	v_add_u32_e32 v92, 0x2200, v91
	v_add_u32_e32 v93, 0x4400, v91
	v_add_u32_e32 v94, 0x6600, v91
	v_add_u32_e32 v95, 0x8800, v91
	v_add_u32_e32 v96, 0xaa00, v91
	v_add_u32_e32 v97, 0xcc00, v91
	v_add_u32_e32 v98, 0xee00, v91
	s_movk_i32 s9, 0xff00
	s_and_b32 s10, s4, 0xffffff00
	s_brev_b32 s11, 1
	s_mov_b32 s12, 0x7c7d7e7f
	s_mov_b32 s13, 0x74757677
	s_mov_b32 s14, 0x6c6d6e6f
	s_mov_b32 s15, 0x64656667
	s_mov_b32 s16, 0x5c5d5e5f
	s_mov_b32 s17, 0x54555657
	s_mov_b32 s18, 0x4c4d4e4f
	s_mov_b32 s19, 0x44454647
	s_mov_b32 s20, 0x3c3d3e3f
	s_mov_b32 s21, 0x34353637
	s_mov_b32 s22, 0x2c2d2e2f
	s_mov_b32 s23, 0x24252627
	s_mov_b32 s24, 0x1c1d1e1f
	s_mov_b32 s25, 0x14151617
	s_mov_b32 s26, 0xc0d0e0f
	s_mov_b32 s27, 0x4050607
	v_mbcnt_hi_u32_b32 v99, -1, v0
	s_movk_i32 s28, 0x7f
	s_movk_i32 s29, 0xff80
	s_movk_i32 s30, 0xff
	v_mov_b32_e32 v100, 0x7060500
	v_mov_b32_e32 v101, 0x7060501
	v_mov_b32_e32 v102, 0x7060502
	v_mov_b32_e32 v103, 0x7060503
	v_bfrev_b32_e32 v104, 1
	.p2align	6

; template <class Epi, class Sched, bool ALIGN_EPI = false, bool SP2 = false>
; __device__ __forceinline__ void gemm_phase(PG8_LAS unsigned char* lds, const Gemm g, const Sched& S, const Epi& E) {
;     ...
;     for (;;) {
;         const bool has_next = S.next(ui + 1, nxt);
;         const char* nA = has_next ? (const char*)g.A + (size_t)nxt.pm * tstep : cA; const char* nB = has_next ? (const char*)g.Bt + (size_t)nxt.pn * tstep : cB;
;         for (int t = 0; t < nt; t += 2) {
;     ...
; #pragma unroll
;         for (int a = 0; a < 2; ++a)
; #pragma unroll
;             for (int b = 0; b < 2; ++b)
; #pragma unroll
;                 for (int m = 0; m < 4; ++m)
; #pragma unroll
;                     for (int n = 0; n < 2; ++n) acc[a][b][m][n] = (f32x4){0.f, 0.f, 0.f, 0.f};
;         cur = nxt; cA = nA; cB = nB; ++ui;
.LBB0_1084:
	s_ashr_i32 s23, s22, 31
	s_lshl_b64 s[24:25], s[22:23], 19
	s_add_u32 s24, s84, s24
	s_addc_u32 s25, s85, s25
	s_and_b64 s[26:27], s[2:3], exec
	s_cselect_b32 s1, s25, s7
	s_cselect_b32 s5, s24, s6
	s_ashr_i32 s21, s20, 31
	s_lshl_b64 s[26:27], s[20:21], 19
	s_add_u32 s26, s30, s26
	s_addc_u32 s27, s31, s27
	s_and_b64 s[28:29], s[2:3], exec
	s_cselect_b32 s21, s27, s9
	s_cselect_b32 s23, s26, s8
	s_add_u32 s6, s6, 0x40080
	s_addc_u32 s7, s7, 0
	s_add_u32 s60, s8, 0x100
	v_mov_b32_e32 v0, 0
	s_addc_u32 s61, s9, 0
	s_mov_b32 s62, -2
	v_mov_b32_e32 v1, v0
	v_mov_b32_e32 v2, v0
	v_mov_b32_e32 v3, v0
	v_mov_b32_e32 v4, v0
	v_mov_b32_e32 v5, v0
	v_mov_b32_e32 v6, v0
	v_mov_b32_e32 v7, v0
	s_waitcnt vmcnt(0)
	v_mov_b32_e32 v16, v0
	v_mov_b32_e32 v17, v0
	v_mov_b32_e32 v18, v0
	v_mov_b32_e32 v19, v0
	v_mov_b32_e32 v20, v0
	v_mov_b32_e32 v21, v0
	v_mov_b32_e32 v22, v0
	v_mov_b32_e32 v23, v0
	v_mov_b32_e32 v32, v0
	v_mov_b32_e32 v33, v0
	v_mov_b32_e32 v34, v0
	v_mov_b32_e32 v35, v0
	v_mov_b32_e32 v36, v0
	v_mov_b32_e32 v37, v0
	v_mov_b32_e32 v38, v0
	v_mov_b32_e32 v39, v0
	v_mov_b32_e32 v48, v0
	v_mov_b32_e32 v49, v0
	v_mov_b32_e32 v50, v0
	v_mov_b32_e32 v51, v0
	v_mov_b32_e32 v52, v0
	v_mov_b32_e32 v53, v0
	v_mov_b32_e32 v54, v0
	v_mov_b32_e32 v55, v0
	v_mov_b32_e32 v8, v0
	v_mov_b32_e32 v9, v0
	v_mov_b32_e32 v10, v0
	v_mov_b32_e32 v11, v0
	v_mov_b32_e32 v12, v0
	v_mov_b32_e32 v13, v0
	v_mov_b32_e32 v14, v0
	v_mov_b32_e32 v15, v0
	v_mov_b32_e32 v24, v0
	v_mov_b32_e32 v25, v0
	v_mov_b32_e32 v26, v0
	v_mov_b32_e32 v27, v0
	v_mov_b32_e32 v28, v0
	v_mov_b32_e32 v29, v0
	v_mov_b32_e32 v30, v0
	v_mov_b32_e32 v31, v0
	v_mov_b32_e32 v40, v0
	v_mov_b32_e32 v41, v0
	v_mov_b32_e32 v42, v0
	v_mov_b32_e32 v43, v0
	v_mov_b32_e32 v44, v0
	v_mov_b32_e32 v45, v0
	v_mov_b32_e32 v46, v0
	v_mov_b32_e32 v47, v0
	v_mov_b32_e32 v56, v0
	v_mov_b32_e32 v57, v0
	v_mov_b32_e32 v58, v0
	v_mov_b32_e32 v59, v0
	v_mov_b32_e32 v60, v0
	v_mov_b32_e32 v61, v0
	v_mov_b32_e32 v62, v0
	v_mov_b32_e32 v63, v0
	v_mov_b32_e32 v64, v0
	v_mov_b32_e32 v65, v0
	v_mov_b32_e32 v66, v0
	v_mov_b32_e32 v67, v0
	v_mov_b32_e32 v68, v0
	v_mov_b32_e32 v69, v0
	v_mov_b32_e32 v70, v0
	v_mov_b32_e32 v71, v0
	v_mov_b32_e32 v80, v0
	v_mov_b32_e32 v81, v0
	v_mov_b32_e32 v82, v0
	v_mov_b32_e32 v83, v0
	v_mov_b32_e32 v84, v0
	v_mov_b32_e32 v85, v0
	v_mov_b32_e32 v86, v0
	v_mov_b32_e32 v87, v0
	v_mov_b32_e32 v96, v0
	v_mov_b32_e32 v97, v0
	v_mov_b32_e32 v98, v0
	v_mov_b32_e32 v99, v0
	v_mov_b32_e32 v100, v0
	v_mov_b32_e32 v101, v0
	v_mov_b32_e32 v102, v0
	v_mov_b32_e32 v103, v0
	v_mov_b32_e32 v112, v0
	v_mov_b32_e32 v113, v0
	v_mov_b32_e32 v114, v0
	v_mov_b32_e32 v115, v0
	v_mov_b32_e32 v116, v0
	v_mov_b32_e32 v117, v0
	v_mov_b32_e32 v118, v0
	v_mov_b32_e32 v119, v0
	v_mov_b32_e32 v72, v0
	v_mov_b32_e32 v73, v0
	v_mov_b32_e32 v74, v0
	v_mov_b32_e32 v75, v0
	v_mov_b32_e32 v76, v0
	v_mov_b32_e32 v77, v0
	v_mov_b32_e32 v78, v0
	v_mov_b32_e32 v79, v0
	v_mov_b32_e32 v88, v0
	v_mov_b32_e32 v89, v0
	v_mov_b32_e32 v90, v0
	v_mov_b32_e32 v91, v0
	v_mov_b32_e32 v92, v0
	v_mov_b32_e32 v93, v0
	v_mov_b32_e32 v94, v0
	v_mov_b32_e32 v95, v0
	v_mov_b32_e32 v104, v0
	v_mov_b32_e32 v105, v0
	v_mov_b32_e32 v106, v0
	v_mov_b32_e32 v107, v0
	v_mov_b32_e32 v108, v0
	v_mov_b32_e32 v109, v0
	v_mov_b32_e32 v110, v0
	v_mov_b32_e32 v111, v0
	v_mov_b32_e32 v120, v0
	v_mov_b32_e32 v121, v0
	v_mov_b32_e32 v122, v0
	v_mov_b32_e32 v123, v0
	v_mov_b32_e32 v124, v0
	v_mov_b32_e32 v125, v0
	v_mov_b32_e32 v126, v0
	v_mov_b32_e32 v127, v0
	.p2align	6

; template <class Epi, class Sched, bool ALIGN_EPI = false, bool SP2 = false>
; __device__ __forceinline__ void gemm_phase(PG8_LAS unsigned char* lds, const Gemm g, const Sched& S, const Epi& E) {
;     ...
;     for (;;) {
;         const bool has_next = S.next(ui + 1, nxt);
;         const char* nA = has_next ? (const char*)g.A + (size_t)nxt.pm * tstep : cA; const char* nB = has_next ? (const char*)g.Bt + (size_t)nxt.pn * tstep : cB;
;         for (int t = 0; t < nt; t += 2) {
;     ...
; #pragma unroll
;         for (int a = 0; a < 2; ++a)
; #pragma unroll
;             for (int b = 0; b < 2; ++b)
; #pragma unroll
;                 for (int m = 0; m < 4; ++m)
; #pragma unroll
;                     for (int n = 0; n < 2; ++n) acc[a][b][m][n] = (f32x4){0.f, 0.f, 0.f, 0.f};
;         cur = nxt; cA = nA; cB = nB; ++ui;
.LBB0_1421:
	s_ashr_i32 s19, s18, 31
	s_lshl_b64 s[20:21], s[18:19], 19
	v_readlane_b32 s22, v237, 45
	v_readlane_b32 s23, v237, 46
	s_add_u32 s20, s22, s20
	s_addc_u32 s21, s23, s21
	s_and_b64 s[22:23], s[4:5], exec
	s_cselect_b32 s19, s21, s27
	s_cselect_b32 s25, s20, s26
	s_ashr_i32 s17, s16, 31
	s_lshl_b64 s[22:23], s[16:17], 19
	s_add_u32 s22, s33, s22
	s_addc_u32 s23, s34, s23
	s_and_b64 s[30:31], s[4:5], exec
	s_cselect_b32 s17, s23, s29
	s_cselect_b32 s48, s22, s28
	s_add_u32 s26, s26, 0x40080
	s_addc_u32 s27, s27, 0
	s_add_u32 s49, s28, 0x100
	v_mov_b32_e32 v0, 0
	s_addc_u32 s50, s29, 0
	s_mov_b32 s51, -2
	s_waitcnt lgkmcnt(0)
	v_mov_b32_e32 v1, v0
	v_mov_b32_e32 v2, v0
	v_mov_b32_e32 v3, v0
	v_mov_b32_e32 v4, v0
	v_mov_b32_e32 v5, v0
	v_mov_b32_e32 v6, v0
	v_mov_b32_e32 v7, v0
	s_waitcnt vmcnt(0)
	v_mov_b32_e32 v16, v0
	v_mov_b32_e32 v17, v0
	v_mov_b32_e32 v18, v0
	v_mov_b32_e32 v19, v0
	v_mov_b32_e32 v20, v0
	v_mov_b32_e32 v21, v0
	v_mov_b32_e32 v22, v0
	v_mov_b32_e32 v23, v0
	v_mov_b32_e32 v32, v0
	v_mov_b32_e32 v33, v0
	v_mov_b32_e32 v34, v0
	v_mov_b32_e32 v35, v0
	v_mov_b32_e32 v36, v0
	v_mov_b32_e32 v37, v0
	v_mov_b32_e32 v38, v0
	v_mov_b32_e32 v39, v0
	v_mov_b32_e32 v48, v0
	v_mov_b32_e32 v49, v0
	v_mov_b32_e32 v50, v0
	v_mov_b32_e32 v51, v0
	v_mov_b32_e32 v52, v0
	v_mov_b32_e32 v53, v0
	v_mov_b32_e32 v54, v0
	v_mov_b32_e32 v55, v0
	v_mov_b32_e32 v8, v0
	v_mov_b32_e32 v9, v0
	v_mov_b32_e32 v10, v0
	v_mov_b32_e32 v11, v0
	v_mov_b32_e32 v12, v0
	v_mov_b32_e32 v13, v0
	v_mov_b32_e32 v14, v0
	v_mov_b32_e32 v15, v0
	v_mov_b32_e32 v24, v0
	v_mov_b32_e32 v25, v0
	v_mov_b32_e32 v26, v0
	v_mov_b32_e32 v27, v0
	v_mov_b32_e32 v28, v0
	v_mov_b32_e32 v29, v0
	v_mov_b32_e32 v30, v0
	v_mov_b32_e32 v31, v0
	v_mov_b32_e32 v40, v0
	v_mov_b32_e32 v41, v0
	v_mov_b32_e32 v42, v0
	v_mov_b32_e32 v43, v0
	v_mov_b32_e32 v44, v0
	v_mov_b32_e32 v45, v0
	v_mov_b32_e32 v46, v0
	v_mov_b32_e32 v47, v0
	v_mov_b32_e32 v56, v0
	v_mov_b32_e32 v57, v0
	v_mov_b32_e32 v58, v0
	v_mov_b32_e32 v59, v0
	v_mov_b32_e32 v60, v0
	v_mov_b32_e32 v61, v0
	v_mov_b32_e32 v62, v0
	v_mov_b32_e32 v63, v0
	v_mov_b32_e32 v64, v0
	v_mov_b32_e32 v65, v0
	v_mov_b32_e32 v66, v0
	v_mov_b32_e32 v67, v0
	v_mov_b32_e32 v68, v0
	v_mov_b32_e32 v69, v0
	v_mov_b32_e32 v70, v0
	v_mov_b32_e32 v71, v0
	v_mov_b32_e32 v80, v0
	v_mov_b32_e32 v81, v0
	v_mov_b32_e32 v82, v0
	v_mov_b32_e32 v83, v0
	v_mov_b32_e32 v84, v0
	v_mov_b32_e32 v85, v0
	v_mov_b32_e32 v86, v0
	v_mov_b32_e32 v87, v0
	v_mov_b32_e32 v96, v0
	v_mov_b32_e32 v97, v0
	v_mov_b32_e32 v98, v0
	v_mov_b32_e32 v99, v0
	v_mov_b32_e32 v100, v0
	v_mov_b32_e32 v101, v0
	v_mov_b32_e32 v102, v0
	v_mov_b32_e32 v103, v0
	v_mov_b32_e32 v112, v0
	v_mov_b32_e32 v113, v0
	v_mov_b32_e32 v114, v0
	v_mov_b32_e32 v115, v0
	v_mov_b32_e32 v116, v0
	v_mov_b32_e32 v117, v0
	v_mov_b32_e32 v118, v0
	v_mov_b32_e32 v119, v0
	v_mov_b32_e32 v72, v0
	v_mov_b32_e32 v73, v0
	v_mov_b32_e32 v74, v0
	v_mov_b32_e32 v75, v0
	v_mov_b32_e32 v76, v0
	v_mov_b32_e32 v77, v0
	v_mov_b32_e32 v78, v0
	v_mov_b32_e32 v79, v0
	v_mov_b32_e32 v88, v0
	v_mov_b32_e32 v89, v0
	v_mov_b32_e32 v90, v0
	v_mov_b32_e32 v91, v0
	v_mov_b32_e32 v92, v0
	v_mov_b32_e32 v93, v0
	v_mov_b32_e32 v94, v0
	v_mov_b32_e32 v95, v0
	v_mov_b32_e32 v104, v0
	v_mov_b32_e32 v105, v0
	v_mov_b32_e32 v106, v0
	v_mov_b32_e32 v107, v0
	v_mov_b32_e32 v108, v0
	v_mov_b32_e32 v109, v0
	v_mov_b32_e32 v110, v0
	v_mov_b32_e32 v111, v0
	v_mov_b32_e32 v120, v0
	v_mov_b32_e32 v121, v0
	v_mov_b32_e32 v122, v0
	v_mov_b32_e32 v123, v0
	v_mov_b32_e32 v124, v0
	v_mov_b32_e32 v125, v0
	v_mov_b32_e32 v126, v0
	v_mov_b32_e32 v127, v0
	.p2align	6

; #define LAS __attribute__((address_space(3)))
; __device__ __forceinline__ int opaque_i(int v) { asm volatile("" : "+v"(v)); return v; }
; __device__ __forceinline__ void phase_topk(Frame& F, const bf16_t* QP, const bf16_t* K1B, const bf16_t* K2B, unsigned short* EID, float* GATE) {
;     const int lane = opaque_i(F.lane), r32 = lane & 31, hi = lane >> 5, b = (int)blockIdx.x, h = b & 7, nbh = F.G >> 3;
;     { u32x4 kv[8];
; #pragma unroll
;       for (int k = 0; k < 8; ++k) { const int c = F.tid + k * (NWAVES * 64), sub = c >> 11, n = (c >> 4) & 127, part = c & 15; kv[k] = *(const u32x4*)((sub ? K2B : K1B) + ((size_t)h * 128 + n) * 128 + 8 * part); }
; #pragma unroll
;       for (int k = 0; k < 8; ++k) { const int c = F.tid + k * (NWAVES * 64), sub = c >> 11, n = (c >> 4) & 127, part = c & 15; *(LAS u32x4*)(F.lds + sub * TK_KSET + n * TK_KSTRIDE + 16 * part) = kv[k]; } }
;     __syncthreads();
;     LAS unsigned* I1s = (LAS unsigned*)(F.lds + TK_KBYTES + F.wave * 8192); LAS unsigned* I2s = I1s + 1024;
;     bf16x8 qn[8];
;     { const int tile0 = (b >> 3) + nbh * F.wave; const bf16_t* qrow = QP + (size_t)((tile0 < TOK / 32 ? tile0 : 0) * 32 + r32) * 2048 + h * 256 + 8 * hi;
; #pragma unroll
;       for (int kk = 0; kk < 8; ++kk) qn[kk] = *(const bf16x8*)(qrow + 16 * kk); }
;     for (int tile = (b >> 3) + nbh * F.wave; tile < TOK / 32; tile += nbh * NWAVES) {
;         const int t = tile * 32 + r32;
;         unsigned V1[16], V2[16]; unsigned h4 = (unsigned)hi << 2; asm volatile("" : "+v"(h4));
; #pragma unroll
.LBB0_1578:
	v_readlane_b32 s2, v237, 4
	v_readlane_b32 s3, v237, 5
	s_cmp_lt_i32 s2, 16
	s_cselect_b64 s[2:3], -1, 0
	s_and_b64 s[0:1], s[2:3], s[0:1]
	s_andn2_b64 vcc, exec, s[0:1]
	s_cbranch_vccnz .LBB0_1582
	s_add_u32 s2, s78, 0x1840000
	s_addc_u32 s3, s79, 0
	s_add_u32 s8, s78, 0x18c0000
	v_readlane_b32 s11, v237, 3
	s_addc_u32 s9, s79, 0
	s_and_b32 s4, s11, 7
	s_lshl_b32 s5, s4, 14
	s_waitcnt lgkmcnt(0)
	v_and_b32_e32 v1, 0x1f80, v184
	v_or_b32_e32 v1, s5, v1
	s_waitcnt vmcnt(0)
	v_lshlrev_b32_e32 v30, 1, v1
	v_mov_b32_e32 v31, 0
	v_lshl_add_u64 v[2:3], s[2:3], 0, v[30:31]
	v_and_b32_e32 v34, 0xf0, v183
	v_mov_b32_e32 v35, v31
	v_add_u32_e32 v1, 0x200, v209
	v_lshl_add_u64 v[10:11], v[2:3], 0, v[34:35]
	v_lshlrev_b32_e32 v2, 3, v1
	v_and_b32_e32 v2, 0x3f80, v2
	v_or_b32_e32 v2, s5, v2
	s_movk_i32 s10, 0x200
	v_lshlrev_b32_e32 v2, 1, v2
	v_mov_b32_e32 v3, v31
	v_mov_b32_e32 v0, v208
	v_lshl_add_u64 v[2:3], s[2:3], 0, v[2:3]
	v_or_b32_e32 v36, 0x400, v209
	v_mov_b32_e32 v14, s9
	v_mov_b32_e32 v15, s3
	v_cmp_gt_u32_e32 vcc, s10, v209
	v_lshl_add_u64 v[12:13], v[2:3], 0, v[34:35]
	global_load_dwordx4 v[2:5], v[10:11], off
	global_load_dwordx4 v[6:9], v[12:13], off
	v_lshlrev_b32_e32 v10, 3, v36
	v_add_u32_e32 v37, 0x600, v209
	v_cndmask_b32_e32 v15, v14, v15, vcc
	v_mov_b32_e32 v14, s8
	v_mov_b32_e32 v16, s2
	v_and_b32_e32 v10, 0x3f80, v10
	v_cndmask_b32_e32 v14, v14, v16, vcc
	v_lshlrev_b32_e32 v16, 3, v37
	v_lshl_add_u64 v[18:19], s[8:9], 0, v[30:31]
	v_add_u32_e32 v38, 0xa00, v209
	v_or_b32_e32 v10, s5, v10
	v_and_b32_e32 v16, 0x3f80, v16
	v_lshl_add_u64 v[26:27], v[18:19], 0, v[34:35]
	v_lshlrev_b32_e32 v18, 3, v38
	v_lshlrev_b32_e32 v10, 1, v10
	v_mov_b32_e32 v11, v31
	v_or_b32_e32 v16, s5, v16
	v_and_b32_e32 v18, 0x3f80, v18
	v_lshl_add_u64 v[10:11], s[2:3], 0, v[10:11]
	v_lshlrev_b32_e32 v16, 1, v16
	v_mov_b32_e32 v17, v31
	v_or_b32_e32 v18, s5, v18
	v_lshl_add_u64 v[10:11], v[10:11], 0, v[34:35]
	v_lshl_add_u64 v[14:15], v[14:15], 0, v[16:17]
	v_lshlrev_b32_e32 v30, 1, v18
	global_load_dwordx4 v[10:13], v[10:11], off
	v_lshl_add_u64 v[14:15], v[14:15], 0, v[34:35]
	v_lshl_add_u64 v[18:19], s[8:9], 0, v[30:31]
	v_or_b32_e32 v39, 0xc00, v209
	global_load_dwordx4 v[14:17], v[14:15], off
	v_lshl_add_u64 v[28:29], v[18:19], 0, v[34:35]
	global_load_dwordx4 v[18:21], v[26:27], off
	global_load_dwordx4 v[22:25], v[28:29], off
	v_lshlrev_b32_e32 v26, 3, v39
	v_and_b32_e32 v26, 0x3f80, v26
	v_or_b32_e32 v26, s5, v26
	v_lshlrev_b32_e32 v30, 1, v26
	v_lshl_add_u64 v[26:27], s[8:9], 0, v[30:31]
	v_add_u32_e32 v40, 0xe00, v209
	v_lshl_add_u64 v[26:27], v[26:27], 0, v[34:35]
	v_lshlrev_b32_e32 v30, 3, v40
	global_load_dwordx4 v[26:29], v[26:27], off
	v_and_b32_e32 v30, 0x3f80, v30
	v_or_b32_e32 v30, s5, v30
	v_lshlrev_b32_e32 v30, 1, v30
	v_lshl_add_u64 v[30:31], s[8:9], 0, v[30:31]
	v_lshl_add_u64 v[30:31], v[30:31], 0, v[34:35]
	global_load_dwordx4 v[30:33], v[30:31], off
	v_lshrrev_b32_e32 v1, 4, v1
	v_mul_u32_u24_e32 v35, 0x110, v182
	v_lshrrev_b32_e32 v36, 4, v36
	v_mul_u32_u24_e32 v1, 0x110, v1
	v_add3_u32 v35, 0, v35, v34
	v_mul_u32_u24_e32 v36, 0x110, v36
	v_add3_u32 v1, 0, v1, v34
	v_add3_u32 v36, 0, v36, v34
	s_mov_b32 s2, 0x8800
	s_ashr_i32 s5, s11, 3
	s_mov_b32 s3, 0
	s_waitcnt vmcnt(7)
	ds_write_b128 v35, v[2:5]
	s_waitcnt vmcnt(6)
	ds_write_b128 v1, v[6:9]
	s_waitcnt vmcnt(5)
	ds_write_b128 v36, v[10:13]
	v_lshrrev_b32_e32 v1, 11, v37
	v_bfe_u32 v2, v37, 4, 7
	v_mad_u32_u24 v1, v1, s2, 0
	v_mul_u32_u24_e32 v2, 0x110, v2
	v_add3_u32 v1, v1, v2, v34
	s_waitcnt vmcnt(4)
	ds_write_b128 v1, v[14:17]
	s_waitcnt vmcnt(3)
	ds_write_b128 v35, v[18:21] offset:34816
	v_bfe_u32 v1, v38, 4, 7
	v_mul_u32_u24_e32 v1, 0x110, v1
	v_add3_u32 v1, 0, v1, v34
	s_waitcnt vmcnt(2)
	ds_write_b128 v1, v[22:25] offset:34816
	v_bfe_u32 v1, v39, 4, 7
	v_mul_u32_u24_e32 v1, 0x110, v1
	v_add3_u32 v1, 0, v1, v34
	v_bfe_u32 v2, v40, 4, 7
	v_mul_u32_u24_e32 v2, 0x110, v2
	s_waitcnt vmcnt(1)
	ds_write_b128 v1, v[26:29] offset:34816
	v_lshrrev_b32_e32 v1, 11, v40
	v_mad_u32_u24 v1, v1, s2, 0
	s_ashr_i32 s2, s72, 3
	s_mul_i32 s2, s2, s74
	s_add_i32 s33, s2, s5
	v_add3_u32 v1, v1, v2, v34
	s_cmpk_gt_i32 s33, 0x3ff
	s_waitcnt vmcnt(0)
	ds_write_b128 v1, v[30:33]
	s_waitcnt lgkmcnt(0)
	s_barrier
	s_cbranch_scc1 .LBB0_1582
	v_and_b32_e32 v88, 31, v0
	v_lshl_or_b32 v80, s33, 5, v88
	v_ashrrev_i32_e32 v1, 5, v0
	v_ashrrev_i32_e32 v81, 31, v80
	v_lshlrev_b32_e32 v2, 3, v1
	v_lshlrev_b64 v[4:5], 12, v[80:81]
	v_ashrrev_i32_e32 v3, 31, v2
	v_lshl_add_u64 v[4:5], s[96:97], 0, v[4:5]
	s_lshl_b32 s2, s4, 9
	v_lshl_add_u64 v[4:5], v[4:5], 0, s[2:3]
	v_lshlrev_b64 v[6:7], 1, v[2:3]
	v_lshl_add_u64 v[4:5], v[4:5], 0, v[6:7]
	global_load_dwordx4 v[16:19], v[4:5], off offset:224
	global_load_dwordx4 v[20:23], v[4:5], off offset:192
	global_load_dwordx4 v[24:27], v[4:5], off offset:160
	global_load_dwordx4 v[28:31], v[4:5], off offset:128
	global_load_dwordx4 v[32:35], v[4:5], off offset:96
	global_load_dwordx4 v[36:39], v[4:5], off offset:64
	global_load_dwordx4 v[40:43], v[4:5], off offset:32
	global_load_dwordx4 v[44:47], v[4:5], off
	s_lshl_b32 s3, s74, 13
	s_add_i32 s3, s3, 0
	s_add_i32 s3, s3, 0x11000
	s_and_b32 s8, s72, -8
	s_add_u32 s10, s96, s2
	s_addc_u32 s11, s97, 0
	s_lshl_b32 s5, s4, 5
	v_readlane_b32 s12, v236, 3
	v_readlane_b32 s13, v236, 4
	s_add_u32 s12, s12, s5
	s_addc_u32 s13, s13, 0
	s_lshl_b32 s4, s4, 6
	v_readlane_b32 s5, v236, 14
	s_add_u32 s4, s5, s4
	v_readlane_b32 s5, v236, 17
	v_lshlrev_b32_e32 v89, 2, v1
	v_lshlrev_b32_e32 v1, 4, v1
	v_lshl_add_u32 v90, v0, 2, s3
	v_cmp_gt_u32_e64 s[2:3], 32, v0
	s_addc_u32 s5, s5, 0
	v_mul_u32_u24_e32 v0, 0x110, v88
	v_lshl_add_u64 v[84:85], v[2:3], 2, s[4:5]
	v_add3_u32 v91, 0, v0, v1
	s_lshl_b32 s4, s72, 5
	v_mbcnt_lo_u32_b32 v0, -1, 0
	v_lshl_add_u64 v[82:83], s[12:13], 0, v[6:7]
	v_lshl_add_u64 v[86:87], s[10:11], 0, v[6:7]
	v_add_u32_e32 v92, 0x2200, v91
	v_add_u32_e32 v93, 0x4400, v91
	v_add_u32_e32 v94, 0x6600, v91
	v_add_u32_e32 v95, 0x8800, v91
	v_add_u32_e32 v96, 0xaa00, v91
	v_add_u32_e32 v97, 0xcc00, v91
	v_add_u32_e32 v98, 0xee00, v91
	s_movk_i32 s9, 0xff00
	s_and_b32 s10, s4, 0xffffff00
	s_brev_b32 s11, 1
	s_mov_b32 s12, 0x7c7d7e7f
	s_mov_b32 s13, 0x74757677
	s_mov_b32 s14, 0x6c6d6e6f
	s_mov_b32 s15, 0x64656667
	s_mov_b32 s16, 0x5c5d5e5f
	s_mov_b32 s17, 0x54555657
	s_mov_b32 s18, 0x4c4d4e4f
	s_mov_b32 s19, 0x44454647
	s_mov_b32 s20, 0x3c3d3e3f
	s_mov_b32 s21, 0x34353637
	s_mov_b32 s22, 0x2c2d2e2f
	s_mov_b32 s23, 0x24252627
	s_mov_b32 s24, 0x1c1d1e1f
	s_mov_b32 s25, 0x14151617
	s_mov_b32 s26, 0xc0d0e0f
	s_mov_b32 s27, 0x4050607
	v_mbcnt_hi_u32_b32 v99, -1, v0
	s_movk_i32 s28, 0x7f
	s_movk_i32 s29, 0xff80
	s_movk_i32 s30, 0xff
	v_mov_b32_e32 v100, 0x7060500
	v_mov_b32_e32 v101, 0x7060501
	v_mov_b32_e32 v102, 0x7060502
	v_mov_b32_e32 v103, 0x7060503
	v_bfrev_b32_e32 v104, 1
	.p2align	6
